# 8-byte instruction phase of the G1, attention tile and G3 loops set to the phase with fewer misaligned 64-bit encodings (4-byte pads)
# speedup vs baseline: 1.0088x; 1.0088x over previous
.LBB0_246:
	s_ashr_i32 s43, s42, 31
	v_cmp_lt_i64_e32 vcc, s[8:9], v[180:181]
	s_lshl_b64 s[8:9], s[42:43], 19
	s_add_u32 s44, s26, s8
	s_addc_u32 s45, s27, s9
	s_and_b64 s[8:9], vcc, exec
	s_cselect_b32 s8, s45, s51
	s_cselect_b32 s9, s44, s50
	s_ashr_i32 s5, s4, 31
	s_lshl_b64 s[46:47], s[4:5], 19
	s_add_u32 s46, s37, s46
	s_addc_u32 s47, s54, s47
	s_and_b64 s[52:53], vcc, exec
	s_cselect_b32 s5, s47, s49
	s_cselect_b32 s43, s46, s48
	s_add_u32 s67, s50, 0x100
	s_addc_u32 s72, s51, 0
	s_add_u32 s48, s48, 0x80
	v_mov_b32_e32 v4, 0
	s_addc_u32 s49, s49, 0
	s_mov_b32 s73, -2
	v_mov_b32_e32 v5, v4
	v_mov_b32_e32 v6, v4
	v_mov_b32_e32 v7, v4
	v_mov_b32_e32 v8, v4
	v_mov_b32_e32 v9, v4
	v_mov_b32_e32 v10, v4
	v_mov_b32_e32 v11, v4
	v_mov_b32_e32 v12, v4
	v_mov_b32_e32 v13, v4
	v_mov_b32_e32 v14, v4
	v_mov_b32_e32 v15, v4
	v_mov_b32_e32 v20, v4
	v_mov_b32_e32 v21, v4
	v_mov_b32_e32 v22, v4
	v_mov_b32_e32 v23, v4
	v_mov_b32_e32 v28, v4
	v_mov_b32_e32 v29, v4
	v_mov_b32_e32 v30, v4
	v_mov_b32_e32 v31, v4
	v_mov_b32_e32 v36, v4
	v_mov_b32_e32 v37, v4
	v_mov_b32_e32 v38, v4
	v_mov_b32_e32 v39, v4
	v_mov_b32_e32 v44, v4
	v_mov_b32_e32 v45, v4
	v_mov_b32_e32 v46, v4
	v_mov_b32_e32 v47, v4
	v_mov_b32_e32 v52, v4
	v_mov_b32_e32 v53, v4
	v_mov_b32_e32 v54, v4
	v_mov_b32_e32 v55, v4
	v_mov_b32_e32 v16, v4
	v_mov_b32_e32 v17, v4
	v_mov_b32_e32 v18, v4
	v_mov_b32_e32 v19, v4
	v_mov_b32_e32 v24, v4
	v_mov_b32_e32 v25, v4
	v_mov_b32_e32 v26, v4
	v_mov_b32_e32 v27, v4
	v_mov_b32_e32 v32, v4
	v_mov_b32_e32 v33, v4
	v_mov_b32_e32 v34, v4
	v_mov_b32_e32 v35, v4
	v_mov_b32_e32 v40, v4
	v_mov_b32_e32 v41, v4
	v_mov_b32_e32 v42, v4
	v_mov_b32_e32 v43, v4
	v_mov_b32_e32 v48, v4
	v_mov_b32_e32 v49, v4
	v_mov_b32_e32 v50, v4
	v_mov_b32_e32 v51, v4
	v_mov_b32_e32 v56, v4
	v_mov_b32_e32 v57, v4
	v_mov_b32_e32 v58, v4
	v_mov_b32_e32 v59, v4
	v_mov_b32_e32 v60, v4
	v_mov_b32_e32 v61, v4
	v_mov_b32_e32 v62, v4
	v_mov_b32_e32 v63, v4
	v_mov_b32_e32 v64, v4
	v_mov_b32_e32 v65, v4
	v_mov_b32_e32 v66, v4
	v_mov_b32_e32 v67, v4
	v_mov_b32_e32 v68, v4
	v_mov_b32_e32 v69, v4
	v_mov_b32_e32 v70, v4
	v_mov_b32_e32 v71, v4
	v_mov_b32_e32 v72, v4
	v_mov_b32_e32 v73, v4
	v_mov_b32_e32 v74, v4
	v_mov_b32_e32 v75, v4
	v_mov_b32_e32 v76, v4
	v_mov_b32_e32 v77, v4
	v_mov_b32_e32 v78, v4
	v_mov_b32_e32 v79, v4
	v_mov_b32_e32 v84, v4
	v_mov_b32_e32 v85, v4
	v_mov_b32_e32 v86, v4
	v_mov_b32_e32 v87, v4
	v_mov_b32_e32 v92, v4
	v_mov_b32_e32 v93, v4
	v_mov_b32_e32 v94, v4
	v_mov_b32_e32 v95, v4
	v_mov_b32_e32 v100, v4
	v_mov_b32_e32 v101, v4
	v_mov_b32_e32 v102, v4
	v_mov_b32_e32 v103, v4
	v_mov_b32_e32 v108, v4
	v_mov_b32_e32 v109, v4
	v_mov_b32_e32 v110, v4
	v_mov_b32_e32 v111, v4
	v_mov_b32_e32 v116, v4
	v_mov_b32_e32 v117, v4
	v_mov_b32_e32 v118, v4
	v_mov_b32_e32 v119, v4
	v_mov_b32_e32 v80, v4
	v_mov_b32_e32 v81, v4
	v_mov_b32_e32 v82, v4
	v_mov_b32_e32 v83, v4
	v_mov_b32_e32 v88, v4
	v_mov_b32_e32 v89, v4
	v_mov_b32_e32 v90, v4
	v_mov_b32_e32 v91, v4
	v_mov_b32_e32 v96, v4
	v_mov_b32_e32 v97, v4
	v_mov_b32_e32 v98, v4
	v_mov_b32_e32 v99, v4
	v_mov_b32_e32 v104, v4
	v_mov_b32_e32 v105, v4
	v_mov_b32_e32 v106, v4
	v_mov_b32_e32 v107, v4
	v_mov_b32_e32 v112, v4
	v_mov_b32_e32 v113, v4
	v_mov_b32_e32 v114, v4
	v_mov_b32_e32 v115, v4
	v_mov_b32_e32 v120, v4
	v_mov_b32_e32 v121, v4
	v_mov_b32_e32 v122, v4
	v_mov_b32_e32 v123, v4
	v_mov_b32_e32 v124, v4
	v_mov_b32_e32 v125, v4
	v_mov_b32_e32 v126, v4
	v_mov_b32_e32 v127, v4
	v_mov_b32_e32 v128, v4
	v_mov_b32_e32 v129, v4
	v_mov_b32_e32 v130, v4
	v_mov_b32_e32 v131, v4
	s_nop 0

.LBB0_301:
	s_or_b64 exec, exec, s[0:1]
	s_waitcnt lgkmcnt(0)
	s_barrier
	s_nop 0

.LBB0_324:
	v_pk_mul_f32 v[4:5], v[4:5], s[30:31] op_sel_hi:[1,0]
	s_lshl_b32 s6, s62, 13
	s_lshl_b32 s8, s61, 7
	v_mov_b32_e32 v16, v3
	v_mov_b32_e32 v17, v3
	v_cvt_pk_bf16_f32 v177, v4, v5
	s_add_i32 s42, s64, 4
	s_waitcnt vmcnt(0)
	v_mul_f32_e32 v195, 0x3fb8aa3b, v2
	s_lshl_b32 s43, s62, 8
	s_add_i32 s52, s8, s6
	s_lshl_b32 s6, s63, 7
	v_mov_b32_e32 v2, v3
	v_mov_b32_e32 v4, v3
	v_mov_b32_e32 v5, v3
	v_mov_b32_e32 v6, v3
	v_mov_b32_e32 v7, v3
	v_mov_b32_e32 v8, v3
	v_mov_b32_e32 v9, v3
	v_mov_b32_e32 v10, v3
	v_mov_b32_e32 v11, v3
	v_mov_b32_e32 v12, v3
	v_mov_b32_e32 v13, v3
	v_mov_b32_e32 v14, v3
	v_mov_b32_e32 v15, v3
	v_mov_b64_e32 v[32:33], v[16:17]
	v_mov_b64_e32 v[48:49], v[16:17]
	v_mov_b64_e32 v[64:65], v[16:17]
	v_mov_b64_e32 v[80:81], v[16:17]
	s_addk_i32 s43, 0x3e80
	s_addk_i32 s52, 0xff80
	s_max_i32 s53, s42, 1
	v_add_u32_e32 v193, s8, v204
	s_mov_b32 s67, 0
	s_sub_i32 s72, 0, s64
	s_lshl_b32 s6, s6, 1
	v_mov_b64_e32 v[30:31], v[14:15]
	v_mov_b64_e32 v[28:29], v[12:13]
	v_mov_b64_e32 v[26:27], v[10:11]
	v_mov_b64_e32 v[24:25], v[8:9]
	v_mov_b64_e32 v[22:23], v[6:7]
	v_mov_b64_e32 v[20:21], v[4:5]
	v_mov_b64_e32 v[18:19], v[2:3]
	v_mov_b64_e32 v[46:47], v[14:15]
	v_mov_b64_e32 v[44:45], v[12:13]
	v_mov_b64_e32 v[42:43], v[10:11]
	v_mov_b64_e32 v[40:41], v[8:9]
	v_mov_b64_e32 v[38:39], v[6:7]
	v_mov_b64_e32 v[36:37], v[4:5]
	v_mov_b64_e32 v[34:35], v[2:3]
	v_mov_b64_e32 v[62:63], v[14:15]
	v_mov_b64_e32 v[60:61], v[12:13]
	v_mov_b64_e32 v[58:59], v[10:11]
	v_mov_b64_e32 v[56:57], v[8:9]
	v_mov_b64_e32 v[54:55], v[6:7]
	v_mov_b64_e32 v[52:53], v[4:5]
	v_mov_b64_e32 v[50:51], v[2:3]
	v_mov_b64_e32 v[78:79], v[14:15]
	v_mov_b64_e32 v[76:77], v[12:13]
	v_mov_b64_e32 v[74:75], v[10:11]
	v_mov_b64_e32 v[72:73], v[8:9]
	v_mov_b64_e32 v[70:71], v[6:7]
	v_mov_b64_e32 v[68:69], v[4:5]
	v_mov_b64_e32 v[66:67], v[2:3]
	v_mov_b32_e32 v5, v196
	ds_write_b128 v198, v[122:125]
	ds_write_b128 v198, v[126:129] offset:64
	ds_write_b128 v199, v[130:133] offset:34816
	ds_write_b128 v199, v[134:137] offset:34944
	s_waitcnt lgkmcnt(0)
	s_barrier
	s_nop 0

.LBB0_340:
	s_cmp_eq_u32 s53, s67
	s_waitcnt lgkmcnt(0)
	s_barrier
	s_cbranch_scc1 .LBB0_342
	s_waitcnt vmcnt(3)
	v_mov_b64_e32 v[148:149], v[124:125]
	s_waitcnt vmcnt(2)
	v_mov_b64_e32 v[152:153], v[128:129]
	s_waitcnt vmcnt(1)
	v_mov_b64_e32 v[156:157], v[132:133]
	s_waitcnt vmcnt(0)
	v_mov_b64_e32 v[160:161], v[136:137]
	v_mov_b64_e32 v[146:147], v[122:123]
	v_mov_b64_e32 v[150:151], v[126:127]
	v_mov_b64_e32 v[154:155], v[130:131]
	v_mov_b64_e32 v[158:159], v[134:135]
	s_branch .LBB0_325
	s_nop 0

.LBB0_604:
	v_mov_b64_e32 v[4:5], s[6:7]
	s_ashr_i32 s47, s46, 31
	v_cmp_lt_i64_e32 vcc, s[8:9], v[4:5]
	s_lshl_b64 s[8:9], s[46:47], 19
	s_add_u32 s50, s37, s8
	s_addc_u32 s51, s60, s9
	s_and_b64 s[8:9], vcc, exec
	s_cselect_b32 s8, s51, s57
	s_cselect_b32 s9, s50, s56
	s_ashr_i32 s45, s44, 31
	s_lshl_b64 s[52:53], s[44:45], 19
	s_add_u32 s52, s61, s52
	s_addc_u32 s53, s62, s53
	s_and_b64 s[58:59], vcc, exec
	s_cselect_b32 s45, s53, s55
	s_cselect_b32 s47, s52, s54
	s_add_u32 s89, s56, 0x100
	s_addc_u32 s96, s57, 0
	s_add_u32 s54, s54, 0x80
	v_mov_b32_e32 v4, 0
	s_addc_u32 s55, s55, 0
	s_mov_b32 s97, -2
	v_mov_b32_e32 v5, v4
	v_mov_b32_e32 v6, v4
	v_mov_b32_e32 v7, v4
	v_mov_b32_e32 v8, v4
	v_mov_b32_e32 v9, v4
	v_mov_b32_e32 v10, v4
	v_mov_b32_e32 v11, v4
	v_mov_b32_e32 v12, v4
	v_mov_b32_e32 v13, v4
	v_mov_b32_e32 v14, v4
	v_mov_b32_e32 v15, v4
	v_mov_b32_e32 v20, v4
	v_mov_b32_e32 v21, v4
	v_mov_b32_e32 v22, v4
	v_mov_b32_e32 v23, v4
	v_mov_b32_e32 v28, v4
	v_mov_b32_e32 v29, v4
	v_mov_b32_e32 v30, v4
	v_mov_b32_e32 v31, v4
	v_mov_b32_e32 v36, v4
	v_mov_b32_e32 v37, v4
	v_mov_b32_e32 v38, v4
	v_mov_b32_e32 v39, v4
	v_mov_b32_e32 v44, v4
	v_mov_b32_e32 v45, v4
	v_mov_b32_e32 v46, v4
	v_mov_b32_e32 v47, v4
	v_mov_b32_e32 v52, v4
	v_mov_b32_e32 v53, v4
	v_mov_b32_e32 v54, v4
	v_mov_b32_e32 v55, v4
	v_mov_b32_e32 v16, v4
	v_mov_b32_e32 v17, v4
	v_mov_b32_e32 v18, v4
	v_mov_b32_e32 v19, v4
	v_mov_b32_e32 v24, v4
	v_mov_b32_e32 v25, v4
	v_mov_b32_e32 v26, v4
	v_mov_b32_e32 v27, v4
	v_mov_b32_e32 v32, v4
	v_mov_b32_e32 v33, v4
	v_mov_b32_e32 v34, v4
	v_mov_b32_e32 v35, v4
	v_mov_b32_e32 v40, v4
	v_mov_b32_e32 v41, v4
	v_mov_b32_e32 v42, v4
	v_mov_b32_e32 v43, v4
	v_mov_b32_e32 v48, v4
	v_mov_b32_e32 v49, v4
	v_mov_b32_e32 v50, v4
	v_mov_b32_e32 v51, v4
	v_mov_b32_e32 v56, v4
	v_mov_b32_e32 v57, v4
	v_mov_b32_e32 v58, v4
	v_mov_b32_e32 v59, v4
	v_mov_b32_e32 v60, v4
	v_mov_b32_e32 v61, v4
	v_mov_b32_e32 v62, v4
	v_mov_b32_e32 v63, v4
	v_mov_b32_e32 v64, v4
	v_mov_b32_e32 v65, v4
	v_mov_b32_e32 v66, v4
	v_mov_b32_e32 v67, v4
	v_mov_b32_e32 v68, v4
	v_mov_b32_e32 v69, v4
	v_mov_b32_e32 v70, v4
	v_mov_b32_e32 v71, v4
	v_mov_b32_e32 v72, v4
	v_mov_b32_e32 v73, v4
	v_mov_b32_e32 v74, v4
	v_mov_b32_e32 v75, v4
	v_mov_b32_e32 v76, v4
	v_mov_b32_e32 v77, v4
	v_mov_b32_e32 v78, v4
	v_mov_b32_e32 v79, v4
	v_mov_b32_e32 v84, v4
	v_mov_b32_e32 v85, v4
	v_mov_b32_e32 v86, v4
	v_mov_b32_e32 v87, v4
	v_mov_b32_e32 v92, v4
	v_mov_b32_e32 v93, v4
	v_mov_b32_e32 v94, v4
	v_mov_b32_e32 v95, v4
	v_mov_b32_e32 v100, v4
	v_mov_b32_e32 v101, v4
	v_mov_b32_e32 v102, v4
	v_mov_b32_e32 v103, v4
	v_mov_b32_e32 v108, v4
	v_mov_b32_e32 v109, v4
	v_mov_b32_e32 v110, v4
	v_mov_b32_e32 v111, v4
	v_mov_b32_e32 v116, v4
	v_mov_b32_e32 v117, v4
	v_mov_b32_e32 v118, v4
	v_mov_b32_e32 v119, v4
	v_mov_b32_e32 v80, v4
	v_mov_b32_e32 v81, v4
	v_mov_b32_e32 v82, v4
	v_mov_b32_e32 v83, v4
	v_mov_b32_e32 v88, v4
	v_mov_b32_e32 v89, v4
	v_mov_b32_e32 v90, v4
	v_mov_b32_e32 v91, v4
	v_mov_b32_e32 v96, v4
	v_mov_b32_e32 v97, v4
	v_mov_b32_e32 v98, v4
	v_mov_b32_e32 v99, v4
	v_mov_b32_e32 v104, v4
	v_mov_b32_e32 v105, v4
	v_mov_b32_e32 v106, v4
	v_mov_b32_e32 v107, v4
	v_mov_b32_e32 v112, v4
	v_mov_b32_e32 v113, v4
	v_mov_b32_e32 v114, v4
	v_mov_b32_e32 v115, v4
	v_mov_b32_e32 v120, v4
	v_mov_b32_e32 v121, v4
	v_mov_b32_e32 v122, v4
	v_mov_b32_e32 v123, v4
	v_mov_b32_e32 v124, v4
	v_mov_b32_e32 v125, v4
	v_mov_b32_e32 v126, v4
	v_mov_b32_e32 v127, v4
	v_mov_b32_e32 v128, v4
	v_mov_b32_e32 v129, v4
	v_mov_b32_e32 v130, v4
	v_mov_b32_e32 v131, v4
	s_nop 0
.LBB0_605:
	s_add_u32 s56, s54, 0x80
	s_addc_u32 s57, s55, 0
	s_add_i32 vcc_lo, 0, 0x10000
	v_add_u32_e32 v220, vcc_lo, v145
	v_add_u32_e32 v221, vcc_lo, v146
	ds_read_b128 v[150:153], v220
	ds_read_b128 v[158:161], v220 offset:2048
	ds_read_b128 v[154:157], v221
	ds_read_b128 v[162:165], v221 offset:2048
	s_cmp_eq_u32 s97, 12
	s_cselect_b32 s59, s45, s57
	s_cselect_b32 s58, s47, s56
	s_cselect_b32 s57, s8, s96
	s_cselect_b32 s56, s9, s89
	s_add_i32 s76, s31, s64
	v_lshl_add_u64 v[142:143], s[54:55], 0, v[140:141]
	s_mov_b32 m0, s76
	ds_read_b128 v[166:169], v148
	ds_read_b128 v[182:185], v148 offset:2048
	ds_read_b128 v[170:173], v149
	ds_read_b128 v[186:189], v149 offset:2048
	ds_read_b128 v[190:193], v148 offset:4096
	ds_read_b128 v[198:201], v148 offset:6144
	ds_read_b128 v[194:197], v149 offset:4096
	ds_read_b128 v[202:205], v149 offset:6144
	global_load_lds_dwordx4 v[142:143], off
	v_lshl_add_u64 v[142:143], s[54:55], 0, v[138:139]
	s_add_i32 m0, s76, 0x2000
	s_nop 0
	global_load_lds_dwordx4 v[142:143], off
	s_waitcnt vmcnt(6)
	s_waitcnt lgkmcnt(0)
	s_barrier
	s_setprio 1
	s_waitcnt lgkmcnt(0)
	v_mfma_scale_f32_16x16x128_f8f6f4 v[128:131], v[150:157], v[166:173], v[128:131], v1, v1 op_sel_hi:[0,0,0]
	v_mfma_scale_f32_16x16x128_f8f6f4 v[124:127], v[158:165], v[166:173], v[124:127], v1, v1 op_sel_hi:[0,0,0]
	v_mfma_scale_f32_16x16x128_f8f6f4 v[120:123], v[150:157], v[182:189], v[120:123], v1, v1 op_sel_hi:[0,0,0]
	v_mfma_scale_f32_16x16x128_f8f6f4 v[112:115], v[158:165], v[182:189], v[112:115], v1, v1 op_sel_hi:[0,0,0]
	v_mfma_scale_f32_16x16x128_f8f6f4 v[104:107], v[150:157], v[190:197], v[104:107], v1, v1 op_sel_hi:[0,0,0]
	v_mfma_scale_f32_16x16x128_f8f6f4 v[96:99], v[158:165], v[190:197], v[96:99], v1, v1 op_sel_hi:[0,0,0]
	v_mfma_scale_f32_16x16x128_f8f6f4 v[88:91], v[150:157], v[198:205], v[88:91], v1, v1 op_sel_hi:[0,0,0]
	v_mfma_scale_f32_16x16x128_f8f6f4 v[80:83], v[158:165], v[198:205], v[80:83], v1, v1 op_sel_hi:[0,0,0]
	s_setprio 0
	s_barrier
	s_add_i32 s76, 0, 0x14000
	v_add_u32_e32 v142, s76, v145
	v_add_u32_e32 v143, s76, v146
	s_mov_b32 m0, s5
	ds_read_b128 v[150:153], v142
	ds_read_b128 v[158:161], v142 offset:2048
	ds_read_b128 v[154:157], v143
	ds_read_b128 v[162:165], v143 offset:2048
	v_lshl_add_u64 v[142:143], s[56:57], 0, v[2:3]
	global_load_lds_dwordx4 v[142:143], off
	v_lshl_add_u64 v[174:175], s[56:57], 0, v[134:135]
	s_mov_b32 m0, s43
	s_nop 0
	global_load_lds_dwordx4 v[174:175], off
	s_waitcnt vmcnt(6)
	s_waitcnt lgkmcnt(0)
	s_barrier
	s_setprio 1
	s_waitcnt lgkmcnt(0)
	v_mfma_scale_f32_16x16x128_f8f6f4 v[116:119], v[150:157], v[166:173], v[116:119], v1, v1 op_sel_hi:[0,0,0]
	v_mfma_scale_f32_16x16x128_f8f6f4 v[108:111], v[158:165], v[166:173], v[108:111], v1, v1 op_sel_hi:[0,0,0]
	v_mfma_scale_f32_16x16x128_f8f6f4 v[100:103], v[150:157], v[182:189], v[100:103], v1, v1 op_sel_hi:[0,0,0]
	v_mfma_scale_f32_16x16x128_f8f6f4 v[92:95], v[158:165], v[182:189], v[92:95], v1, v1 op_sel_hi:[0,0,0]
	v_mfma_scale_f32_16x16x128_f8f6f4 v[84:87], v[150:157], v[190:197], v[84:87], v1, v1 op_sel_hi:[0,0,0]
	v_mfma_scale_f32_16x16x128_f8f6f4 v[76:79], v[158:165], v[190:197], v[76:79], v1, v1 op_sel_hi:[0,0,0]
	v_mfma_scale_f32_16x16x128_f8f6f4 v[72:75], v[150:157], v[198:205], v[72:75], v1, v1 op_sel_hi:[0,0,0]
	v_mfma_scale_f32_16x16x128_f8f6f4 v[68:71], v[158:165], v[198:205], v[68:71], v1, v1 op_sel_hi:[0,0,0]
	s_setprio 0
	s_barrier
	s_add_u32 s80, s58, 0x40000
	s_addc_u32 s81, s59, 0
	s_add_i32 s76, s76, s64
	v_lshl_add_u64 v[176:177], s[80:81], 0, v[136:137]
	s_mov_b32 m0, s76
	ds_read_b128 v[166:169], v148 offset:16384
	ds_read_b128 v[182:185], v148 offset:18432
	ds_read_b128 v[170:173], v149 offset:16384
	ds_read_b128 v[186:189], v149 offset:18432
	ds_read_b128 v[190:193], v148 offset:20480
	ds_read_b128 v[198:201], v148 offset:22528
	ds_read_b128 v[194:197], v149 offset:20480
	ds_read_b128 v[202:205], v149 offset:22528
	global_load_lds_dwordx4 v[176:177], off
	v_lshl_add_u64 v[176:177], s[80:81], 0, v[132:133]
	s_add_i32 m0, s76, 0x2000
	s_nop 0
	global_load_lds_dwordx4 v[176:177], off
	s_waitcnt vmcnt(6)
	s_waitcnt lgkmcnt(0)
	s_barrier
	s_setprio 1
	s_waitcnt lgkmcnt(0)
	v_mfma_scale_f32_16x16x128_f8f6f4 v[52:55], v[150:157], v[166:173], v[52:55], v1, v1 op_sel_hi:[0,0,0]
	v_mfma_scale_f32_16x16x128_f8f6f4 v[44:47], v[158:165], v[166:173], v[44:47], v1, v1 op_sel_hi:[0,0,0]
	v_mfma_scale_f32_16x16x128_f8f6f4 v[36:39], v[150:157], v[182:189], v[36:39], v1, v1 op_sel_hi:[0,0,0]
	v_mfma_scale_f32_16x16x128_f8f6f4 v[28:31], v[158:165], v[182:189], v[28:31], v1, v1 op_sel_hi:[0,0,0]
	v_mfma_scale_f32_16x16x128_f8f6f4 v[20:23], v[150:157], v[190:197], v[20:23], v1, v1 op_sel_hi:[0,0,0]
	v_mfma_scale_f32_16x16x128_f8f6f4 v[12:15], v[158:165], v[190:197], v[12:15], v1, v1 op_sel_hi:[0,0,0]
	v_mfma_scale_f32_16x16x128_f8f6f4 v[8:11], v[150:157], v[198:205], v[8:11], v1, v1 op_sel_hi:[0,0,0]
	v_mfma_scale_f32_16x16x128_f8f6f4 v[4:7], v[158:165], v[198:205], v[4:7], v1, v1 op_sel_hi:[0,0,0]
	s_setprio 0
	s_barrier
	s_add_u32 s80, s56, 0x40000
	s_addc_u32 s81, s57, 0
	s_mov_b32 m0, s66
	v_lshl_add_u64 v[176:177], s[80:81], 0, v[2:3]
	ds_read_b128 v[150:153], v220
	ds_read_b128 v[158:161], v220 offset:2048
	ds_read_b128 v[154:157], v221
	ds_read_b128 v[162:165], v221 offset:2048
	global_load_lds_dwordx4 v[176:177], off
	v_lshl_add_u64 v[176:177], s[80:81], 0, v[134:135]
	s_mov_b32 m0, s67
	s_nop 0
	global_load_lds_dwordx4 v[176:177], off
	s_waitcnt vmcnt(6)
	s_waitcnt lgkmcnt(0)
	s_barrier
	s_setprio 1
	s_waitcnt lgkmcnt(0)
	v_mfma_scale_f32_16x16x128_f8f6f4 v[64:67], v[150:157], v[166:173], v[64:67], v1, v1 op_sel_hi:[0,0,0]
	v_mfma_scale_f32_16x16x128_f8f6f4 v[60:63], v[158:165], v[166:173], v[60:63], v1, v1 op_sel_hi:[0,0,0]
	v_mfma_scale_f32_16x16x128_f8f6f4 v[56:59], v[150:157], v[182:189], v[56:59], v1, v1 op_sel_hi:[0,0,0]
	v_mfma_scale_f32_16x16x128_f8f6f4 v[48:51], v[158:165], v[182:189], v[48:51], v1, v1 op_sel_hi:[0,0,0]
	v_mfma_scale_f32_16x16x128_f8f6f4 v[40:43], v[150:157], v[190:197], v[40:43], v1, v1 op_sel_hi:[0,0,0]
	v_mfma_scale_f32_16x16x128_f8f6f4 v[32:35], v[158:165], v[190:197], v[32:35], v1, v1 op_sel_hi:[0,0,0]
	v_mfma_scale_f32_16x16x128_f8f6f4 v[24:27], v[150:157], v[198:205], v[24:27], v1, v1 op_sel_hi:[0,0,0]
	v_mfma_scale_f32_16x16x128_f8f6f4 v[16:19], v[158:165], v[198:205], v[16:19], v1, v1 op_sel_hi:[0,0,0]
	s_setprio 0
	s_barrier
	v_add_u32_e32 v220, s31, v145
	v_add_u32_e32 v221, s31, v146
	ds_read_b128 v[150:153], v220
	ds_read_b128 v[158:161], v220 offset:2048
	ds_read_b128 v[154:157], v221
	ds_read_b128 v[162:165], v221 offset:2048
	s_add_i32 s76, vcc_lo, s64
	v_lshl_add_u64 v[176:177], s[58:59], 0, v[136:137]
	s_mov_b32 m0, s76
	ds_read_b128 v[166:169], v148 offset:32768
	ds_read_b128 v[182:185], v148 offset:34816
	ds_read_b128 v[170:173], v149 offset:32768
	ds_read_b128 v[186:189], v149 offset:34816
	ds_read_b128 v[190:193], v148 offset:36864
	ds_read_b128 v[198:201], v148 offset:38912
	ds_read_b128 v[194:197], v149 offset:36864
	ds_read_b128 v[202:205], v149 offset:38912
	global_load_lds_dwordx4 v[176:177], off
	v_lshl_add_u64 v[176:177], s[58:59], 0, v[132:133]
	s_add_i32 m0, s76, 0x2000
	s_nop 0
	global_load_lds_dwordx4 v[176:177], off
	s_waitcnt vmcnt(6)
	s_waitcnt lgkmcnt(0)
	s_barrier
	s_setprio 1
	s_waitcnt lgkmcnt(0)
	v_mfma_scale_f32_16x16x128_f8f6f4 v[128:131], v[150:157], v[166:173], v[128:131], v1, v1 op_sel_hi:[0,0,0]
	v_mfma_scale_f32_16x16x128_f8f6f4 v[124:127], v[158:165], v[166:173], v[124:127], v1, v1 op_sel_hi:[0,0,0]
	v_mfma_scale_f32_16x16x128_f8f6f4 v[120:123], v[150:157], v[182:189], v[120:123], v1, v1 op_sel_hi:[0,0,0]
	v_mfma_scale_f32_16x16x128_f8f6f4 v[112:115], v[158:165], v[182:189], v[112:115], v1, v1 op_sel_hi:[0,0,0]
	v_mfma_scale_f32_16x16x128_f8f6f4 v[104:107], v[150:157], v[190:197], v[104:107], v1, v1 op_sel_hi:[0,0,0]
	v_mfma_scale_f32_16x16x128_f8f6f4 v[96:99], v[158:165], v[190:197], v[96:99], v1, v1 op_sel_hi:[0,0,0]
	v_mfma_scale_f32_16x16x128_f8f6f4 v[88:91], v[150:157], v[198:205], v[88:91], v1, v1 op_sel_hi:[0,0,0]
	v_mfma_scale_f32_16x16x128_f8f6f4 v[80:83], v[158:165], v[198:205], v[80:83], v1, v1 op_sel_hi:[0,0,0]
	s_setprio 0
	s_barrier
	s_add_i32 s76, 0, 0x1c000
	s_mov_b32 m0, s72
	v_add_u32_e32 v154, s76, v145
	v_add_u32_e32 v162, s76, v146
	v_lshl_add_u64 v[142:143], v[142:143], 0, s[20:21]
	ds_read_b128 v[150:153], v154
	ds_read_b128 v[158:161], v154 offset:2048
	ds_read_b128 v[154:157], v162
	ds_read_b128 v[162:165], v162 offset:2048
	global_load_lds_dwordx4 v[142:143], off
	v_lshl_add_u64 v[142:143], v[174:175], 0, s[20:21]
	s_mov_b32 m0, s73
	s_nop 0
	global_load_lds_dwordx4 v[142:143], off
	s_waitcnt vmcnt(6)
	s_waitcnt lgkmcnt(0)
	s_barrier
	s_setprio 1
	s_waitcnt lgkmcnt(0)
	v_mfma_scale_f32_16x16x128_f8f6f4 v[116:119], v[150:157], v[166:173], v[116:119], v1, v1 op_sel_hi:[0,0,0]
	v_mfma_scale_f32_16x16x128_f8f6f4 v[108:111], v[158:165], v[166:173], v[108:111], v1, v1 op_sel_hi:[0,0,0]
	v_mfma_scale_f32_16x16x128_f8f6f4 v[100:103], v[150:157], v[182:189], v[100:103], v1, v1 op_sel_hi:[0,0,0]
	v_mfma_scale_f32_16x16x128_f8f6f4 v[92:95], v[158:165], v[182:189], v[92:95], v1, v1 op_sel_hi:[0,0,0]
	v_mfma_scale_f32_16x16x128_f8f6f4 v[84:87], v[150:157], v[190:197], v[84:87], v1, v1 op_sel_hi:[0,0,0]
	v_mfma_scale_f32_16x16x128_f8f6f4 v[76:79], v[158:165], v[190:197], v[76:79], v1, v1 op_sel_hi:[0,0,0]
	v_mfma_scale_f32_16x16x128_f8f6f4 v[72:75], v[150:157], v[198:205], v[72:75], v1, v1 op_sel_hi:[0,0,0]
	v_mfma_scale_f32_16x16x128_f8f6f4 v[68:71], v[158:165], v[198:205], v[68:71], v1, v1 op_sel_hi:[0,0,0]
	s_setprio 0
	s_barrier
	s_add_u32 s58, s58, 0x40080
	s_addc_u32 s59, s59, 0
	s_add_i32 s76, s76, s64
	v_lshl_add_u64 v[142:143], s[58:59], 0, v[136:137]
	s_mov_b32 m0, s76
	ds_read_b128 v[166:169], v148 offset:49152
	ds_read_b128 v[182:185], v148 offset:51200
	ds_read_b128 v[170:173], v149 offset:49152
	ds_read_b128 v[186:189], v149 offset:51200
	ds_read_b128 v[190:193], v148 offset:53248
	ds_read_b128 v[198:201], v148 offset:55296
	ds_read_b128 v[194:197], v149 offset:53248
	ds_read_b128 v[202:205], v149 offset:55296
	global_load_lds_dwordx4 v[142:143], off
	v_lshl_add_u64 v[142:143], s[58:59], 0, v[132:133]
	s_add_i32 m0, s76, 0x2000
	s_nop 0
	global_load_lds_dwordx4 v[142:143], off
	s_waitcnt vmcnt(6)
	s_waitcnt lgkmcnt(0)
	s_barrier
	s_setprio 1
	s_waitcnt lgkmcnt(0)
	v_mfma_scale_f32_16x16x128_f8f6f4 v[52:55], v[150:157], v[166:173], v[52:55], v1, v1 op_sel_hi:[0,0,0]
	v_mfma_scale_f32_16x16x128_f8f6f4 v[44:47], v[158:165], v[166:173], v[44:47], v1, v1 op_sel_hi:[0,0,0]
	v_mfma_scale_f32_16x16x128_f8f6f4 v[36:39], v[150:157], v[182:189], v[36:39], v1, v1 op_sel_hi:[0,0,0]
	v_mfma_scale_f32_16x16x128_f8f6f4 v[28:31], v[158:165], v[182:189], v[28:31], v1, v1 op_sel_hi:[0,0,0]
	v_mfma_scale_f32_16x16x128_f8f6f4 v[20:23], v[150:157], v[190:197], v[20:23], v1, v1 op_sel_hi:[0,0,0]
	v_mfma_scale_f32_16x16x128_f8f6f4 v[12:15], v[158:165], v[190:197], v[12:15], v1, v1 op_sel_hi:[0,0,0]
	v_mfma_scale_f32_16x16x128_f8f6f4 v[8:11], v[150:157], v[198:205], v[8:11], v1, v1 op_sel_hi:[0,0,0]
	v_mfma_scale_f32_16x16x128_f8f6f4 v[4:7], v[158:165], v[198:205], v[4:7], v1, v1 op_sel_hi:[0,0,0]
	s_setprio 0
	s_barrier
	s_add_u32 s56, s56, 0x40080
	s_addc_u32 s57, s57, 0
	s_mov_b32 m0, s74
	v_lshl_add_u64 v[142:143], s[56:57], 0, v[2:3]
	ds_read_b128 v[150:153], v220
	ds_read_b128 v[158:161], v220 offset:2048
	ds_read_b128 v[154:157], v221
	ds_read_b128 v[162:165], v221 offset:2048
	global_load_lds_dwordx4 v[142:143], off
	v_lshl_add_u64 v[142:143], s[56:57], 0, v[134:135]
	s_mov_b32 m0, s75
	s_nop 0
	global_load_lds_dwordx4 v[142:143], off
	s_waitcnt vmcnt(6)
	s_waitcnt lgkmcnt(0)
	s_barrier
	s_setprio 1
	s_waitcnt lgkmcnt(0)
	v_mfma_scale_f32_16x16x128_f8f6f4 v[64:67], v[150:157], v[166:173], v[64:67], v1, v1 op_sel_hi:[0,0,0]
	v_mfma_scale_f32_16x16x128_f8f6f4 v[60:63], v[158:165], v[166:173], v[60:63], v1, v1 op_sel_hi:[0,0,0]
	v_mfma_scale_f32_16x16x128_f8f6f4 v[56:59], v[150:157], v[182:189], v[56:59], v1, v1 op_sel_hi:[0,0,0]
	v_mfma_scale_f32_16x16x128_f8f6f4 v[48:51], v[158:165], v[182:189], v[48:51], v1, v1 op_sel_hi:[0,0,0]
	v_mfma_scale_f32_16x16x128_f8f6f4 v[40:43], v[150:157], v[190:197], v[40:43], v1, v1 op_sel_hi:[0,0,0]
	v_mfma_scale_f32_16x16x128_f8f6f4 v[32:35], v[158:165], v[190:197], v[32:35], v1, v1 op_sel_hi:[0,0,0]
	v_mfma_scale_f32_16x16x128_f8f6f4 v[24:27], v[150:157], v[198:205], v[24:27], v1, v1 op_sel_hi:[0,0,0]
	v_mfma_scale_f32_16x16x128_f8f6f4 v[16:19], v[158:165], v[198:205], v[16:19], v1, v1 op_sel_hi:[0,0,0]
	s_setprio 0
	s_barrier
	s_add_i32 s97, s97, 2
	s_add_u32 s89, s89, 0x100
	s_addc_u32 s96, s96, 0
	s_add_u32 s54, s54, 0x100
	s_addc_u32 s55, s55, 0
	s_cmp_gt_u32 s97, 13
	s_cbranch_scc0 .LBB0_605
	v_lshl_add_u32 v150, s42, 8, v144
	v_lshl_or_b32 v142, s4, 8, v147
	v_ashrrev_i32_e32 v151, 31, v150
	v_ashrrev_i32_e32 v143, 31, v142
	v_lshlrev_b64 v[152:153], 12, v[150:151]
	v_lshl_add_u64 v[152:153], s[0:1], 0, v[152:153]
	v_lshlrev_b64 v[154:155], 1, v[142:143]
	v_lshl_add_u64 v[142:143], v[152:153], 0, v[154:155]
	v_pk_mul_f32 v[130:131], v[130:131], s[22:23] op_sel_hi:[1,0]
	v_pk_mul_f32 v[128:129], v[128:129], s[22:23] op_sel_hi:[1,0]
	v_pk_mul_f32 v[152:153], v[126:127], s[22:23] op_sel_hi:[1,0]
	v_pk_mul_f32 v[126:127], v[124:125], s[22:23] op_sel_hi:[1,0]
	v_cvt_pk_bf16_f32 v124, v128, v129
	v_cvt_pk_bf16_f32 v125, v130, v131
	v_cvt_pk_bf16_f32 v126, v126, v127
	v_cvt_pk_bf16_f32 v127, v152, v153
	global_store_dwordx4 v[142:143], v[124:127], off
	v_pk_mul_f32 v[118:119], v[118:119], s[22:23] op_sel_hi:[1,0]
	v_pk_mul_f32 v[116:117], v[116:117], s[22:23] op_sel_hi:[1,0]
	v_pk_mul_f32 v[124:125], v[110:111], s[22:23] op_sel_hi:[1,0]
	v_pk_mul_f32 v[110:111], v[108:109], s[22:23] op_sel_hi:[1,0]
	v_cvt_pk_bf16_f32 v108, v116, v117
	v_cvt_pk_bf16_f32 v109, v118, v119
	v_cvt_pk_bf16_f32 v110, v110, v111
	v_cvt_pk_bf16_f32 v111, v124, v125
	global_store_dwordx4 v[142:143], v[108:111], off offset:256
	v_pk_mul_f32 v[114:115], v[114:115], s[22:23] op_sel_hi:[1,0]
	v_pk_mul_f32 v[112:113], v[112:113], s[22:23] op_sel_hi:[1,0]
	v_or_b32_e32 v108, 16, v150
	v_ashrrev_i32_e32 v109, 31, v108
	v_lshlrev_b64 v[108:109], 12, v[108:109]
	v_lshl_add_u64 v[108:109], s[0:1], 0, v[108:109]
	v_lshl_add_u64 v[116:117], v[108:109], 0, v[154:155]
	v_pk_mul_f32 v[110:111], v[122:123], s[22:23] op_sel_hi:[1,0]
	v_pk_mul_f32 v[108:109], v[120:121], s[22:23] op_sel_hi:[1,0]
	v_pk_mul_f32 v[102:103], v[102:103], s[22:23] op_sel_hi:[1,0]
	v_cvt_pk_bf16_f32 v108, v108, v109
	v_cvt_pk_bf16_f32 v109, v110, v111
	v_cvt_pk_bf16_f32 v110, v112, v113
	v_cvt_pk_bf16_f32 v111, v114, v115
	global_store_dwordx4 v[116:117], v[108:111], off
	v_pk_mul_f32 v[100:101], v[100:101], s[22:23] op_sel_hi:[1,0]
	v_pk_mul_f32 v[98:99], v[98:99], s[22:23] op_sel_hi:[1,0]
	v_pk_mul_f32 v[108:109], v[94:95], s[22:23] op_sel_hi:[1,0]
	v_pk_mul_f32 v[94:95], v[92:93], s[22:23] op_sel_hi:[1,0]
	v_cvt_pk_bf16_f32 v92, v100, v101
	v_cvt_pk_bf16_f32 v93, v102, v103
	v_cvt_pk_bf16_f32 v94, v94, v95
	v_cvt_pk_bf16_f32 v95, v108, v109
	global_store_dwordx4 v[116:117], v[92:95], off offset:256
	v_pk_mul_f32 v[96:97], v[96:97], s[22:23] op_sel_hi:[1,0]
	v_pk_mul_f32 v[86:87], v[86:87], s[22:23] op_sel_hi:[1,0]
	v_or_b32_e32 v92, 32, v150
	v_ashrrev_i32_e32 v93, 31, v92
	v_lshlrev_b64 v[92:93], 12, v[92:93]
	v_lshl_add_u64 v[92:93], s[0:1], 0, v[92:93]
	v_lshl_add_u64 v[100:101], v[92:93], 0, v[154:155]
	v_pk_mul_f32 v[94:95], v[106:107], s[22:23] op_sel_hi:[1,0]
	v_pk_mul_f32 v[92:93], v[104:105], s[22:23] op_sel_hi:[1,0]
	v_pk_mul_f32 v[84:85], v[84:85], s[22:23] op_sel_hi:[1,0]
	v_cvt_pk_bf16_f32 v92, v92, v93
	v_cvt_pk_bf16_f32 v93, v94, v95
	v_cvt_pk_bf16_f32 v94, v96, v97
	v_cvt_pk_bf16_f32 v95, v98, v99
	global_store_dwordx4 v[100:101], v[92:95], off
	v_pk_mul_f32 v[82:83], v[82:83], s[22:23] op_sel_hi:[1,0]
	v_pk_mul_f32 v[80:81], v[80:81], s[22:23] op_sel_hi:[1,0]
	v_pk_mul_f32 v[92:93], v[78:79], s[22:23] op_sel_hi:[1,0]
	v_pk_mul_f32 v[78:79], v[76:77], s[22:23] op_sel_hi:[1,0]
	v_cvt_pk_bf16_f32 v76, v84, v85
	v_cvt_pk_bf16_f32 v77, v86, v87
	v_cvt_pk_bf16_f32 v78, v78, v79
	v_cvt_pk_bf16_f32 v79, v92, v93
	global_store_dwordx4 v[100:101], v[76:79], off offset:256
	v_pk_mul_f32 v[74:75], v[74:75], s[22:23] op_sel_hi:[1,0]
	v_pk_mul_f32 v[72:73], v[72:73], s[22:23] op_sel_hi:[1,0]
	v_or_b32_e32 v76, 48, v150
	v_ashrrev_i32_e32 v77, 31, v76
	v_lshlrev_b64 v[76:77], 12, v[76:77]
	v_lshl_add_u64 v[76:77], s[0:1], 0, v[76:77]
	v_lshl_add_u64 v[84:85], v[76:77], 0, v[154:155]
	v_pk_mul_f32 v[78:79], v[90:91], s[22:23] op_sel_hi:[1,0]
	v_pk_mul_f32 v[76:77], v[88:89], s[22:23] op_sel_hi:[1,0]
	v_pk_mul_f32 v[64:65], v[64:65], s[22:23] op_sel_hi:[1,0]
	v_cvt_pk_bf16_f32 v76, v76, v77
	v_cvt_pk_bf16_f32 v77, v78, v79
	v_cvt_pk_bf16_f32 v78, v80, v81
	v_cvt_pk_bf16_f32 v79, v82, v83
	global_store_dwordx4 v[84:85], v[76:79], off
	s_mov_b32 s4, 0x80000
	v_pk_mul_f32 v[66:67], v[66:67], s[22:23] op_sel_hi:[1,0]
	v_pk_mul_f32 v[76:77], v[70:71], s[22:23] op_sel_hi:[1,0]
	v_pk_mul_f32 v[70:71], v[68:69], s[22:23] op_sel_hi:[1,0]
	v_cvt_pk_bf16_f32 v68, v72, v73
	v_cvt_pk_bf16_f32 v69, v74, v75
	v_cvt_pk_bf16_f32 v70, v70, v71
	v_cvt_pk_bf16_f32 v71, v76, v77
	global_store_dwordx4 v[84:85], v[68:71], off offset:256
	s_mov_b64 s[8:9], 0x80000
	v_pk_mul_f32 v[54:55], v[54:55], s[22:23] op_sel_hi:[1,0]
	v_pk_mul_f32 v[70:71], v[62:63], s[22:23] op_sel_hi:[1,0]
	v_pk_mul_f32 v[62:63], v[60:61], s[22:23] op_sel_hi:[1,0]
	v_cvt_pk_bf16_f32 v60, v64, v65
	v_add_co_u32_e32 v64, vcc, s4, v142
	v_cvt_pk_bf16_f32 v61, v66, v67
	v_cvt_pk_bf16_f32 v62, v62, v63
	v_cvt_pk_bf16_f32 v63, v70, v71
	v_addc_co_u32_e32 v65, vcc, 0, v143, vcc
	global_store_dwordx4 v[64:65], v[60:63], off
	v_pk_mul_f32 v[52:53], v[52:53], s[22:23] op_sel_hi:[1,0]
	v_lshl_add_u64 v[68:69], v[142:143], 0, s[8:9]
	v_pk_mul_f32 v[60:61], v[46:47], s[22:23] op_sel_hi:[1,0]
	v_pk_mul_f32 v[46:47], v[44:45], s[22:23] op_sel_hi:[1,0]
	v_cvt_pk_bf16_f32 v44, v52, v53
	v_cvt_pk_bf16_f32 v45, v54, v55
	v_cvt_pk_bf16_f32 v46, v46, v47
	v_cvt_pk_bf16_f32 v47, v60, v61
	global_store_dwordx4 v[68:69], v[44:47], off offset:256
	v_pk_mul_f32 v[48:49], v[48:49], s[22:23] op_sel_hi:[1,0]
	s_mov_b32 s4, 0x90000
	v_pk_mul_f32 v[46:47], v[58:59], s[22:23] op_sel_hi:[1,0]
	v_pk_mul_f32 v[44:45], v[56:57], s[22:23] op_sel_hi:[1,0]
	v_pk_mul_f32 v[50:51], v[50:51], s[22:23] op_sel_hi:[1,0]
	v_cvt_pk_bf16_f32 v44, v44, v45
	v_cvt_pk_bf16_f32 v45, v46, v47
	v_cvt_pk_bf16_f32 v46, v48, v49
	v_add_co_u32_e32 v48, vcc, s4, v142
	v_cvt_pk_bf16_f32 v47, v50, v51
	s_nop 0
	v_addc_co_u32_e32 v49, vcc, 0, v143, vcc
	s_mov_b64 s[8:9], 0x90000
	global_store_dwordx4 v[48:49], v[44:47], off
	v_pk_mul_f32 v[38:39], v[38:39], s[22:23] op_sel_hi:[1,0]
	v_pk_mul_f32 v[36:37], v[36:37], s[22:23] op_sel_hi:[1,0]
	v_pk_mul_f32 v[44:45], v[30:31], s[22:23] op_sel_hi:[1,0]
	v_pk_mul_f32 v[30:31], v[28:29], s[22:23] op_sel_hi:[1,0]
	v_lshl_add_u64 v[52:53], v[142:143], 0, s[8:9]
	v_cvt_pk_bf16_f32 v28, v36, v37
	v_cvt_pk_bf16_f32 v29, v38, v39
	v_cvt_pk_bf16_f32 v30, v30, v31
	v_cvt_pk_bf16_f32 v31, v44, v45
	global_store_dwordx4 v[52:53], v[28:31], off offset:256
	v_pk_mul_f32 v[32:33], v[32:33], s[22:23] op_sel_hi:[1,0]
	s_mov_b32 s4, 0xa0000
	v_pk_mul_f32 v[30:31], v[42:43], s[22:23] op_sel_hi:[1,0]
	v_pk_mul_f32 v[28:29], v[40:41], s[22:23] op_sel_hi:[1,0]
	v_pk_mul_f32 v[34:35], v[34:35], s[22:23] op_sel_hi:[1,0]
	v_cvt_pk_bf16_f32 v28, v28, v29
	v_cvt_pk_bf16_f32 v29, v30, v31
	v_cvt_pk_bf16_f32 v30, v32, v33
	v_add_co_u32_e32 v32, vcc, s4, v142
	v_cvt_pk_bf16_f32 v31, v34, v35
	s_nop 0
	v_addc_co_u32_e32 v33, vcc, 0, v143, vcc
	s_mov_b64 s[8:9], 0xa0000
	global_store_dwordx4 v[32:33], v[28:31], off
	v_pk_mul_f32 v[22:23], v[22:23], s[22:23] op_sel_hi:[1,0]
	v_pk_mul_f32 v[20:21], v[20:21], s[22:23] op_sel_hi:[1,0]
	v_pk_mul_f32 v[28:29], v[14:15], s[22:23] op_sel_hi:[1,0]
	v_pk_mul_f32 v[14:15], v[12:13], s[22:23] op_sel_hi:[1,0]
	v_lshl_add_u64 v[36:37], v[142:143], 0, s[8:9]
	v_cvt_pk_bf16_f32 v12, v20, v21
	v_cvt_pk_bf16_f32 v13, v22, v23
	v_cvt_pk_bf16_f32 v14, v14, v15
	v_cvt_pk_bf16_f32 v15, v28, v29
	global_store_dwordx4 v[36:37], v[12:15], off offset:256
	v_pk_mul_f32 v[16:17], v[16:17], s[22:23] op_sel_hi:[1,0]
	s_mov_b32 s4, 0xb0000
	v_pk_mul_f32 v[14:15], v[26:27], s[22:23] op_sel_hi:[1,0]
	v_pk_mul_f32 v[12:13], v[24:25], s[22:23] op_sel_hi:[1,0]
	v_pk_mul_f32 v[18:19], v[18:19], s[22:23] op_sel_hi:[1,0]
	v_cvt_pk_bf16_f32 v12, v12, v13
	v_cvt_pk_bf16_f32 v13, v14, v15
	v_cvt_pk_bf16_f32 v14, v16, v17
	v_add_co_u32_e32 v16, vcc, s4, v142
	v_cvt_pk_bf16_f32 v15, v18, v19
	s_nop 0
	v_addc_co_u32_e32 v17, vcc, 0, v143, vcc
	s_mov_b64 s[8:9], 0xb0000
	global_store_dwordx4 v[16:17], v[12:15], off
	v_pk_mul_f32 v[10:11], v[10:11], s[22:23] op_sel_hi:[1,0]
	v_pk_mul_f32 v[8:9], v[8:9], s[22:23] op_sel_hi:[1,0]
	v_pk_mul_f32 v[12:13], v[6:7], s[22:23] op_sel_hi:[1,0]
	v_pk_mul_f32 v[6:7], v[4:5], s[22:23] op_sel_hi:[1,0]
	v_lshl_add_u64 v[20:21], v[142:143], 0, s[8:9]
	v_cvt_pk_bf16_f32 v4, v8, v9
	v_cvt_pk_bf16_f32 v5, v10, v11
	v_cvt_pk_bf16_f32 v6, v6, v7
	v_cvt_pk_bf16_f32 v7, v12, v13
	s_and_b64 vcc, exec, s[40:41]
	s_mov_b32 s4, s44
	s_mov_b32 s42, s46
	s_mov_b64 s[54:55], s[52:53]
	s_mov_b64 s[56:57], s[50:51]
	global_store_dwordx4 v[20:21], v[4:7], off offset:256
	s_cbranch_vccz .LBB0_602
	s_waitcnt vmcnt(0)
	v_readlane_b32 s86, v253, 23
	v_readlane_b32 s88, v253, 25
	s_cmpk_gt_u32 s27, 0xff
	v_readlane_b32 s84, v253, 20
	v_readlane_b32 s76, v253, 22
	v_readlane_b32 s87, v253, 24
	v_readlane_b32 s89, v253, 26
	v_readlane_b32 s85, v253, 21
	s_cbranch_scc1 .LBB0_609
	s_barrier
	s_nop 0
